# strategy 6 (LDS bank conflicts): attention K tile XOR swizzle widened from (row&7) to (row&15) in writers and readers: ds_read_b128 K fragments conflict-free (were 2-way)
# speedup vs baseline: 1.0063x; 1.0053x over previous
; #define LAS __attribute__((address_space(3)))
; __device__ __forceinline__ int v_st(int k, int c) { const int kk = (k & ~0xC) | ((k & 4) << 1) | ((k & 8) >> 1); return ((kk >> 3) * 4 + (c >> 5)) * 512 + ((kk & 7) * 32 + (c & 31)) * 2; }
; __device__ __forceinline__ int v_rd_base(int lane) { return ((lane & 3) << 3) | (((lane >> 2) & 3) << 6) | (((lane >> 4) & 1) << 5) | (((lane >> 5) & 1) << 8); }
; #define ATT_SLOAD(S, k0) do { S##_v0 = *(const bf16x8*)(Vh + (size_t)(k0) * NC); S##_v1 = *(const bf16x8*)(Vh + (size_t)((k0) + 32) * NC); \
;     S##_k0 = *(const bf16x8*)(Kh + (size_t)(k0) * NC); S##_k1 = *(const bf16x8*)(Kh + (size_t)((k0) + 32) * NC); } while (0)
; #define ATT_SWAIT() asm volatile("s_waitcnt vmcnt(4)" ::: "memory")
; __device__ __forceinline__ void qkt(f32x16& p0, f32x16& p1, LAS const unsigned char* Ks, const bf16x8* qr, int r32, int hi) {
;     p0 = f32x16{}; p1 = f32x16{};
; #pragma unroll
;     for (int d0 = 0; d0 < 8; ++d0) { const int cb = (d0 * 16 + hi * 8) * 2;
;         const bf16x8 b0 = *(LAS const bf16x8*)(Ks + ATT_KSWZ(r32, cb));
;         const bf16x8 b1 = *(LAS const bf16x8*)(Ks + ATT_KSWZ(32 + r32, cb));
;         p0 = __builtin_amdgcn_mfma_f32_32x32x16_bf16(b0, qr[d0], p0, 0, 0, 0);
;         p1 = __builtin_amdgcn_mfma_f32_32x32x16_bf16(b1, qr[d0], p1, 0, 0, 0); }
; }
; template <bool MOBA>
; __device__ __forceinline__ void run_unit(const UnitDesc& U, LAS unsigned char* lds, f32x16 (&o)[4], float (&rli)[16]) {
;     ...
;     const int sr = tid >> 4, sc = (tid & 15) * 8, vst0 = v_st(sr, sc), vst1 = v_st(32 + sr, sc), kst0 = ATT_KSWZ(sr, sc * 2), kst1 = ATT_KSWZ(32 + sr, sc * 2);
;     LAS const unsigned char* vb0 = V_lds + v_rd_base(lane);
;     const bf16_t* Kh = U.K + (size_t)(sr + kt0 * KVBLK) * NC + sc; const bf16_t* Vh = U.V + (size_t)(sr + kt0 * KVBLK) * NC + sc;
;     qpos -= kt0 * KVBLK; qlo -= kt0 * KVBLK;
;     bf16x8 sA_v0, sA_v1, sA_k0, sA_k1, sB_v0, sB_v1, sB_k0, sB_k1;
;     ...
;     f32x16 pA0, pA1, pB0, pB1; float mnA, mnB, alA, alB; bf16x8 pa0, pa1, pa2, pa3; const int NT = U.nt - kt0;
;     ATT_SLOAD(sA, 0); ATT_SLOAD(sB, KVBLK); ATT_SWAIT(); ATT_SWRITE(0, sA); __syncthreads();
;     qkt(pA0, pA1, K_lds, qr, r32, hi); ATT_PSM(pA0, pA1, mnA, alA, 0);
.LBB0_626:
	s_lshl_b32 s2, s21, 7
	s_and_b32 s67, s23, 0xffffffe0
	s_mul_hi_u32 s0, s22, 0xe800
	s_mul_i32 s22, s22, 0xe800
	v_readlane_b32 s4, v253, 48
	v_readlane_b32 s5, v253, 49
	s_add_u32 s1, s4, s22
	s_addc_u32 s4, s5, s0
	v_writelane_b32 v254, s2, 51
	s_lshl_b32 s2, s2, 1
	s_add_u32 s0, s1, s2
	v_lshlrev_b32_e32 v24, 3, v4
	s_addc_u32 s1, s4, 0
	v_and_b32_e32 v6, 0x78, v24
	s_add_u32 s4, s0, 0x1000
	v_ashrrev_i32_e32 v5, 4, v4
	v_lshlrev_b32_e32 v22, 1, v6
	v_mov_b64_e32 v[6:7], s[0:1]
	s_mov_b32 s6, 0xe800
	s_addc_u32 s5, s1, 0
	v_mad_i64_i32 v[6:7], s[0:1], v5, s6, v[6:7]
	v_mov_b32_e32 v23, v3
	v_lshl_add_u64 v[188:189], v[6:7], 0, v[22:23]
	v_mov_b64_e32 v[6:7], s[4:5]
	v_mad_i64_i32 v[6:7], s[0:1], v5, s6, v[6:7]
	v_lshl_add_u64 v[190:191], v[6:7], 0, v[22:23]
	s_mov_b32 s0, 0x1d0000
	v_add_co_u32_e32 v6, vcc, s0, v190
	v_and_b32_e32 v23, 0xfffff0, v5
	s_nop 0
	v_addc_co_u32_e32 v7, vcc, 0, v191, vcc
	global_load_dwordx4 v[6:9], v[6:7], off
	s_nop 0
	global_load_dwordx4 v[10:13], v[190:191], off
	global_load_dwordx4 v[14:17], v[188:189], off offset:2048
	v_add_co_u32_e32 v18, vcc, s0, v188
	v_lshlrev_b32_e32 v25, 1, v5
	s_nop 0
	v_addc_co_u32_e32 v19, vcc, 0, v189, vcc
	global_load_dwordx4 v[18:21], v[18:19], off offset:2048
	v_lshrrev_b32_e32 v26, 1, v5
	v_and_b32_e32 v27, 3, v5
	v_add_u32_e32 v28, 32, v5
	v_and_or_b32 v23, v25, 8, v23
	v_and_b32_e32 v52, 31, v4
	v_and_b32_e32 v53, 63, v4
	v_and_b32_e32 v4, 0xf0, v4
	v_bfe_u32 v24, v24, 5, 2
	v_lshlrev_b32_e32 v5, 8, v5
	v_and_or_b32 v25, v26, 4, v27
	v_and_b32_e32 v26, 0xfffff0, v28
	v_lshlrev_b32_e32 v27, 1, v28
	v_lshlrev_b32_e32 v28, 8, v28
	v_lshrrev_b32_e32 v23, 1, v23
	v_and_b32_e32 v29, 48, v22
	v_and_or_b32 v26, v27, 8, v26
	v_bitop3_b32 v5, v22, v5, v4 bitop3:0xde
	v_bitop3_b32 v4, v22, v28, v4 bitop3:0xde
	v_or_b32_e32 v22, v23, v24
	v_lshlrev_b32_e32 v25, 6, v25
	v_lshrrev_b32_e32 v23, 1, v26
	v_add_u32_e32 v214, 0, v4
	v_lshlrev_b32_e32 v4, 9, v22
	v_add_u32_e32 v213, 0, v5
	v_or_b32_e32 v5, v23, v24
	v_or3_b32 v4, v4, v25, v29
	s_mov_b32 s0, 0x3a0000
	v_lshlrev_b32_e32 v5, 9, v5
	v_add_u32_e32 v215, 0, v4
	v_add_co_u32_e32 v4, vcc, s0, v188
	v_or3_b32 v24, v5, v25, v29
	s_nop 0
	v_addc_co_u32_e32 v5, vcc, 0, v189, vcc
	s_mov_b32 s1, 0x570000
	v_add_co_u32_e32 v22, vcc, s1, v188
	v_add_u32_e32 v216, 0, v24
	s_nop 0
	v_addc_co_u32_e32 v23, vcc, 0, v189, vcc
	global_load_dwordx4 v[36:39], v[4:5], off offset:2048
	global_load_dwordx4 v[40:43], v[22:23], off offset:2048
	v_add_co_u32_e32 v4, vcc, s0, v190
	s_movk_i32 s0, 0xf0
	s_nop 0
	v_addc_co_u32_e32 v5, vcc, 0, v191, vcc
	v_add_co_u32_e32 v22, vcc, s1, v190
	v_lshl_add_u32 v62, v52, 8, 0
	s_nop 0
	v_addc_co_u32_e32 v23, vcc, 0, v191, vcc
	global_load_dwordx4 v[44:47], v[4:5], off
	global_load_dwordx4 v[48:51], v[22:23], off
	s_waitcnt vmcnt(4)
	s_waitcnt vmcnt(6)
	ds_write_b128 v215, v[10:13]
	ds_write_b128 v216, v[6:9]
	s_waitcnt vmcnt(5)
	ds_write_b128 v213, v[14:17] offset:32768
	s_waitcnt vmcnt(4)
	ds_write_b128 v214, v[18:21] offset:32768
	v_lshlrev_b32_e32 v12, 4, v52
	v_bitop3_b32 v4, v2, v12, s0 bitop3:0x78
	v_add_u32_e32 v204, v62, v4
	s_waitcnt lgkmcnt(0)
	s_barrier
	ds_read_b128 v[4:7], v204 offset:32768
	ds_read_b128 v[8:11], v204 offset:40960
	s_waitcnt lgkmcnt(1)
	v_mfma_f32_32x32x16_bf16 v[20:35], v[4:7], v[144:147], 0
	v_and_b32_e32 v63, 0xf0, v12
	v_bitop3_b32 v54, v2, v63, 32 bitop3:0x36
	v_add_u32_e32 v208, v62, v54
	ds_read_b128 v[54:57], v208 offset:32768
	ds_read_b128 v[58:61], v208 offset:40960
	s_movk_i32 s0, 0x60
	s_mov_b32 s4, 0x41400000
	v_lshlrev_b32_e32 v201, 2, v1
	s_waitcnt lgkmcnt(2)
	v_mfma_f32_32x32x16_bf16 v[4:19], v[8:11], v[144:147], 0
	s_waitcnt lgkmcnt(1)
	v_mfma_f32_32x32x16_bf16 v[20:35], v[54:57], v[140:143], v[20:35]
	v_bitop3_b32 v54, v2, v63, 64 bitop3:0x36
	v_add_u32_e32 v209, v62, v54
	s_waitcnt lgkmcnt(0)
	v_mfma_f32_32x32x16_bf16 v[4:19], v[58:61], v[140:143], v[4:19]
	ds_read_b128 v[54:57], v209 offset:32768
	ds_read_b128 v[58:61], v209 offset:40960
	s_waitcnt lgkmcnt(1)
	v_mfma_f32_32x32x16_bf16 v[20:35], v[54:57], v[136:139], v[20:35]
	v_bitop3_b32 v54, v2, v63, s0 bitop3:0x36
	v_add_u32_e32 v210, v62, v54
	s_movk_i32 s0, 0x80
	s_waitcnt lgkmcnt(0)
	v_mfma_f32_32x32x16_bf16 v[4:19], v[58:61], v[136:139], v[4:19]
	ds_read_b128 v[54:57], v210 offset:32768
	ds_read_b128 v[58:61], v210 offset:40960
	s_waitcnt lgkmcnt(1)
	v_mfma_f32_32x32x16_bf16 v[20:35], v[54:57], v[132:135], v[20:35]
	v_bitop3_b32 v54, v2, v63, s0 bitop3:0x36
	v_add_u32_e32 v202, v62, v54
	s_movk_i32 s0, 0xa0
	s_waitcnt lgkmcnt(0)
	v_mfma_f32_32x32x16_bf16 v[4:19], v[58:61], v[132:135], v[4:19]
	ds_read_b128 v[54:57], v202 offset:32768
	ds_read_b128 v[58:61], v202 offset:40960
	s_waitcnt lgkmcnt(1)
	v_mfma_f32_32x32x16_bf16 v[20:35], v[54:57], v[128:131], v[20:35]
	v_bitop3_b32 v54, v2, v63, s0 bitop3:0x36
	v_add_u32_e32 v206, v62, v54
	ds_read_b128 v[54:57], v206 offset:32768
	s_lshl_b32 s0, s21, 3
	s_sub_i32 s0, 0xffffffd8, s0
	v_cvt_f32_i32_e32 v64, s0
	s_movk_i32 s0, 0xc0
	s_waitcnt lgkmcnt(1)
	v_mfma_f32_32x32x16_bf16 v[4:19], v[58:61], v[128:131], v[4:19]
	ds_read_b128 v[58:61], v206 offset:40960
	v_div_scale_f32 v67, vcc, v64, s4, v64
	s_waitcnt lgkmcnt(1)
	v_mfma_f32_32x32x16_bf16 v[20:35], v[54:57], v[124:127], v[20:35]
	v_bitop3_b32 v54, v2, v63, s0 bitop3:0x36
	v_add_u32_e32 v212, v62, v54
	v_div_scale_f32 v65, s[0:1], s4, s4, v64
	v_rcp_f32_e32 v66, v65
	ds_read_b128 v[54:57], v212 offset:32768
	s_movk_i32 s0, 0xe0
	s_waitcnt lgkmcnt(1)
; #define LAS __attribute__((address_space(3)))
; __device__ __forceinline__ void qkt(f32x16& p0, f32x16& p1, LAS const unsigned char* Ks, const bf16x8* qr, int r32, int hi) {
;     p0 = f32x16{}; p1 = f32x16{};
; #pragma unroll
;     for (int d0 = 0; d0 < 8; ++d0) { const int cb = (d0 * 16 + hi * 8) * 2;
;         const bf16x8 b0 = *(LAS const bf16x8*)(Ks + ATT_KSWZ(r32, cb));
;         const bf16x8 b1 = *(LAS const bf16x8*)(Ks + ATT_KSWZ(32 + r32, cb));
;         p0 = __builtin_amdgcn_mfma_f32_32x32x16_bf16(b0, qr[d0], p0, 0, 0, 0);
;         p1 = __builtin_amdgcn_mfma_f32_32x32x16_bf16(b1, qr[d0], p1, 0, 0, 0); }
; }
; __device__ __forceinline__ void partialSM(f32x16& p0, f32x16& p1, float& m_reg, float& mn, float& alpha, int dq, float slopeL, bool diag, bool rowmasked) {
;     const float NEG = -__builtin_inff(); const float a0 = -slopeL * (float)dq;
; #pragma unroll
;     for (int r = 0; r < 16; ++r) { const int c = (r & 3) + 8 * (r >> 2);
;         p0[r] = fmaf(p0[r], CS, fmaf(slopeL, (float)c, a0)); p1[r] = fmaf(p1[r], CS, fmaf(slopeL, (float)(c + 32), a0)); }
	v_mfma_f32_32x32x16_bf16 v[4:19], v[58:61], v[124:127], v[4:19]
	v_fma_f32 v58, -v65, v66, 1.0
	v_fmac_f32_e32 v66, v58, v66
	v_mul_f32_e32 v68, v67, v66
	v_fma_f32 v58, -v65, v68, v67
	v_fmac_f32_e32 v68, v58, v66
	ds_read_b128 v[58:61], v212 offset:40960
	v_bitop3_b32 v2, v2, v63, s0 bitop3:0x36
	s_waitcnt lgkmcnt(1)
	v_mfma_f32_32x32x16_bf16 v[20:35], v[54:57], v[120:123], v[20:35]
	v_fma_f32 v54, -v65, v68, v67
	v_div_fmas_f32 v54, v54, v66, v68
	v_add_u32_e32 v211, v62, v2
	v_div_fixup_f32 v64, v54, s4, v64
	ds_read_b128 v[54:57], v211 offset:32768
	s_mov_b32 s0, 0xc2fc0000
	v_cmp_gt_f32_e32 vcc, s0, v64
	v_mov_b32_e32 v2, 0x42800000
	s_and_b64 s[0:1], vcc, exec
	v_cndmask_b32_e32 v2, 0, v2, vcc
	v_add_f32_e32 v2, v64, v2
	s_cselect_b32 s0, 0xffffffc0, 0
	s_add_i32 s13, s67, s20
	s_waitcnt lgkmcnt(1)
	v_mfma_f32_32x32x16_bf16 v[4:19], v[58:61], v[120:123], v[4:19]
	v_exp_f32_e32 v2, v2
	ds_read_b128 v[58:61], v211 offset:40960
	v_or_b32_e32 v200, s13, v52
	v_sub_u32_e32 v1, v200, v201
	v_ldexp_f32 v2, v2, s0
	v_mul_f32_e32 v182, 0x3fb8aa3b, v2
	s_mov_b32 s0, 2.0
	s_waitcnt lgkmcnt(1)
	v_mfma_f32_32x32x16_bf16 v[20:35], v[54:57], v[116:119], v[20:35]
	v_cvt_f32_i32_e32 v54, v1
	s_mov_b32 s1, 0x40400000
	s_cmp_gt_i32 s13, 62
	v_mul_f32_e64 v2, -v182, v54
	v_fma_f32 v56, v182, s0, v2
	v_fma_f32 v57, v182, s1, v2
	s_mov_b32 s0, 0x41000000
	s_mov_b32 s1, 0x41100000
	s_waitcnt lgkmcnt(0)
	v_mfma_f32_32x32x16_bf16 v[4:19], v[58:61], v[116:119], v[4:19]
	v_fma_f32 v58, v182, s0, v2
	v_fma_f32 v59, v182, s1, v2
	s_mov_b32 s0, 0x41200000
	s_mov_b32 s1, 0x41300000
	v_fma_f32 v60, v182, s0, v2
	v_fma_f32 v61, v182, s1, v2
	s_mov_b32 s0, 0x41800000
	s_mov_b32 s1, 0x41880000
	v_pk_fma_f32 v[62:63], v[182:183], s[0:1], v[2:3] op_sel_hi:[0,1,0]
	s_mov_b32 s0, 0x41900000
	v_fma_f32 v55, -v182, v54, v182
	v_mov_b32_e32 v54, v2
	s_mov_b32 s1, 0x41980000
	v_fmac_f32_e32 v54, 0, v182
	v_pk_fma_f32 v[64:65], v[182:183], s[0:1], v[2:3] op_sel_hi:[0,1,0]
	v_pk_fma_f32 v[66:67], v[182:183], s[86:87], v[2:3] op_sel_hi:[0,1,0]
	v_pk_fma_f32 v[68:69], v[182:183], s[88:89], v[2:3] op_sel_hi:[0,1,0]
	v_pk_fma_f32 v[20:21], v[20:21], s[96:97], v[54:55] op_sel_hi:[1,0,1]
	v_pk_fma_f32 v[34:35], v[34:35], s[96:97], v[68:69] op_sel_hi:[1,0,1]
	v_pk_fma_f32 v[32:33], v[32:33], s[96:97], v[66:67] op_sel_hi:[1,0,1]
	v_pk_fma_f32 v[30:31], v[30:31], s[96:97], v[64:65] op_sel_hi:[1,0,1]
	v_pk_fma_f32 v[28:29], v[28:29], s[96:97], v[62:63] op_sel_hi:[1,0,1]
	v_pk_fma_f32 v[26:27], v[26:27], s[96:97], v[60:61] op_sel_hi:[1,0,1]
	v_pk_fma_f32 v[24:25], v[24:25], s[96:97], v[58:59] op_sel_hi:[1,0,1]
	v_pk_fma_f32 v[22:23], v[22:23], s[96:97], v[56:57] op_sel_hi:[1,0,1]
	v_pk_fma_f32 v[54:55], v[182:183], s[90:91], v[2:3] op_sel_hi:[0,1,0]
	v_pk_fma_f32 v[56:57], v[182:183], s[92:93], v[2:3] op_sel_hi:[0,1,0]
	v_pk_fma_f32 v[58:59], v[182:183], s[94:95], v[2:3] op_sel_hi:[0,1,0]
	v_pk_fma_f32 v[60:61], v[182:183], s[68:69], v[2:3] op_sel_hi:[0,1,0]
	v_pk_fma_f32 v[62:63], v[182:183], s[70:71], v[2:3] op_sel_hi:[0,1,0]
	v_pk_fma_f32 v[64:65], v[182:183], s[72:73], v[2:3] op_sel_hi:[0,1,0]
	v_pk_fma_f32 v[66:67], v[182:183], s[74:75], v[2:3] op_sel_hi:[0,1,0]
	v_pk_fma_f32 v[68:69], v[182:183], s[76:77], v[2:3] op_sel_hi:[0,1,0]
	v_pk_fma_f32 v[4:5], v[4:5], s[96:97], v[68:69] op_sel_hi:[1,0,1]
	v_pk_fma_f32 v[18:19], v[18:19], s[96:97], v[66:67] op_sel_hi:[1,0,1]
	v_pk_fma_f32 v[16:17], v[16:17], s[96:97], v[64:65] op_sel_hi:[1,0,1]
	v_pk_fma_f32 v[14:15], v[14:15], s[96:97], v[62:63] op_sel_hi:[1,0,1]
	v_pk_fma_f32 v[12:13], v[12:13], s[96:97], v[60:61] op_sel_hi:[1,0,1]
	v_pk_fma_f32 v[10:11], v[10:11], s[96:97], v[58:59] op_sel_hi:[1,0,1]
	v_pk_fma_f32 v[8:9], v[8:9], s[96:97], v[56:57] op_sel_hi:[1,0,1]
	v_pk_fma_f32 v[6:7], v[6:7], s[96:97], v[54:55] op_sel_hi:[1,0,1]
	s_cbranch_scc1 .LBB0_630
; __device__ __forceinline__ void partialSM(f32x16& p0, f32x16& p1, float& m_reg, float& mn, float& alpha, int dq, float slopeL, bool diag, bool rowmasked) {
;     ...
;     if (diag) { asm volatile("" ::: "memory");
; #pragma unroll
;         for (int r = 0; r < 16; ++r) { const int c = (r & 3) + 8 * (r >> 2); if (c > dq) p0[r] = NEG; if (c + 32 > dq) p1[r] = NEG; } }
	v_cmp_gt_i32_e64 s[62:63], 57, v1
	v_cmp_gt_i32_e64 s[64:65], 58, v1
	v_cmp_gt_i32_e64 s[60:61], 56, v1
	s_and_b64 s[62:63], s[64:65], s[62:63]
	v_cmp_gt_i32_e64 s[58:59], 51, v1
	s_and_b64 s[60:61], s[62:63], s[60:61]
	v_cmp_gt_i32_e64 s[56:57], 50, v1
	s_and_b64 s[58:59], s[60:61], s[58:59]
	v_cmp_gt_i32_e64 s[54:55], 49, v1
	s_and_b64 s[56:57], s[58:59], s[56:57]
	v_cmp_gt_i32_e64 s[52:53], 48, v1
	s_and_b64 s[54:55], s[56:57], s[54:55]
	v_cmp_gt_i32_e64 s[50:51], 43, v1
	s_and_b64 s[52:53], s[54:55], s[52:53]
	v_cmp_gt_i32_e64 s[48:49], 42, v1
	s_and_b64 s[50:51], s[52:53], s[50:51]
	v_cmp_gt_i32_e64 s[46:47], 41, v1
	s_and_b64 s[48:49], s[50:51], s[48:49]
	v_cmp_gt_i32_e64 s[44:45], 40, v1
	s_and_b64 s[46:47], s[48:49], s[46:47]
	v_cmp_gt_i32_e64 s[42:43], 35, v1
	s_and_b64 s[44:45], s[46:47], s[44:45]
	v_cmp_gt_i32_e64 s[40:41], 34, v1
	s_and_b64 s[42:43], s[44:45], s[42:43]
	v_cmp_gt_i32_e64 s[38:39], 33, v1
	s_and_b64 s[40:41], s[42:43], s[40:41]
	v_cmp_gt_i32_e64 s[36:37], 32, v1
	s_and_b64 s[38:39], s[40:41], s[38:39]
	s_and_b64 s[36:37], s[38:39], s[36:37]
	v_cmp_gt_i32_e32 vcc, 0, v1
	v_cmp_gt_i32_e64 s[0:1], 1, v1
	v_cmp_gt_i32_e64 s[6:7], 2, v1
	v_cmp_gt_i32_e64 s[8:9], 3, v1
	v_cmp_gt_i32_e64 s[10:11], 8, v1
	v_cmp_gt_i32_e64 s[14:15], 9, v1
	v_cmp_gt_i32_e64 s[16:17], 10, v1
	v_cmp_gt_i32_e64 s[18:19], 11, v1
	v_cmp_gt_i32_e64 s[20:21], 16, v1
	v_cmp_gt_i32_e64 s[22:23], 17, v1
	v_cmp_gt_i32_e64 s[24:25], 18, v1
	v_cmp_gt_i32_e64 s[26:27], 19, v1
	v_cmp_gt_i32_e64 s[28:29], 24, v1
	v_cmp_gt_i32_e64 s[30:31], 25, v1
	v_cmp_gt_i32_e64 s[34:35], 26, v1
	v_cndmask_b32_e64 v18, v18, v241, s[64:65]
	v_cndmask_b32_e64 v17, v17, v241, s[62:63]
	v_cndmask_b32_e64 v16, v16, v241, s[60:61]
	v_cndmask_b32_e64 v15, v15, v241, s[58:59]
	v_cndmask_b32_e64 v14, v14, v241, s[56:57]
	v_cndmask_b32_e64 v13, v13, v241, s[54:55]
	v_cndmask_b32_e64 v12, v12, v241, s[52:53]
	v_cndmask_b32_e64 v11, v11, v241, s[50:51]
	v_cndmask_b32_e64 v10, v10, v241, s[48:49]
	v_cndmask_b32_e64 v9, v9, v241, s[46:47]
	v_cndmask_b32_e64 v8, v8, v241, s[44:45]
	v_cndmask_b32_e64 v7, v7, v241, s[42:43]
	v_cndmask_b32_e64 v6, v6, v241, s[40:41]
	v_cndmask_b32_e64 v5, v5, v241, s[38:39]
	v_cndmask_b32_e64 v4, v4, v241, s[36:37]
	v_cmp_gt_i32_e64 s[36:37], 27, v1
	v_cmp_gt_i32_e64 s[38:39], 59, v1
	s_and_saveexec_b64 s[4:5], s[38:39]
	v_mov_b32_e32 v19, s85
	s_or_b64 exec, exec, s[4:5]
	s_and_b64 s[34:35], s[36:37], s[34:35]
	s_and_b64 s[30:31], s[34:35], s[30:31]
	s_and_b64 s[28:29], s[30:31], s[28:29]
	s_and_b64 s[26:27], s[28:29], s[26:27]
	s_and_b64 s[24:25], s[26:27], s[24:25]
	s_and_b64 s[22:23], s[24:25], s[22:23]
	s_and_b64 s[20:21], s[22:23], s[20:21]
	s_and_b64 s[18:19], s[20:21], s[18:19]
	s_and_b64 s[16:17], s[18:19], s[16:17]
	s_and_b64 s[14:15], s[16:17], s[14:15]
	s_and_b64 s[10:11], s[14:15], s[10:11]
	s_and_b64 s[8:9], s[10:11], s[8:9]
	s_and_b64 s[6:7], s[8:9], s[6:7]
	s_and_b64 s[0:1], s[6:7], s[0:1]
	s_and_b64 vcc, s[0:1], vcc
	v_cndmask_b32_e64 v34, v34, v241, s[34:35]
	v_cndmask_b32_e64 v33, v33, v241, s[30:31]
	v_cndmask_b32_e64 v32, v32, v241, s[28:29]
	v_cndmask_b32_e64 v31, v31, v241, s[26:27]
	v_cndmask_b32_e64 v30, v30, v241, s[24:25]
	v_cndmask_b32_e64 v29, v29, v241, s[22:23]
	v_cndmask_b32_e64 v28, v28, v241, s[20:21]
	v_cndmask_b32_e64 v27, v27, v241, s[18:19]
	v_cndmask_b32_e64 v26, v26, v241, s[16:17]
	v_cndmask_b32_e64 v25, v25, v241, s[14:15]
	v_cndmask_b32_e64 v24, v24, v241, s[10:11]
	v_cndmask_b32_e64 v23, v23, v241, s[8:9]
	v_cndmask_b32_e64 v22, v22, v241, s[6:7]
	v_cndmask_b32_e64 v21, v21, v241, s[0:1]
	v_cndmask_b32_e32 v20, v20, v241, vcc
	v_cndmask_b32_e64 v35, v35, v241, s[36:37]

; #define LAS __attribute__((address_space(3)))
; __device__ __forceinline__ int v_st(int k, int c) { const int kk = (k & ~0xC) | ((k & 4) << 1) | ((k & 8) >> 1); return ((kk >> 3) * 4 + (c >> 5)) * 512 + ((kk & 7) * 32 + (c & 31)) * 2; }
; __device__ __forceinline__ int v_rd_base(int lane) { return ((lane & 3) << 3) | (((lane >> 2) & 3) << 6) | (((lane >> 4) & 1) << 5) | (((lane >> 5) & 1) << 8); }
; #define ATT_SLOAD(S, k0) do { S##_v0 = *(const bf16x8*)(Vh + (size_t)(k0) * NC); S##_v1 = *(const bf16x8*)(Vh + (size_t)((k0) + 32) * NC); \
;     S##_k0 = *(const bf16x8*)(Kh + (size_t)(k0) * NC); S##_k1 = *(const bf16x8*)(Kh + (size_t)((k0) + 32) * NC); } while (0)
; #define ATT_SWAIT() asm volatile("s_waitcnt vmcnt(4)" ::: "memory")
; __device__ __forceinline__ void qkt(f32x16& p0, f32x16& p1, LAS const unsigned char* Ks, const bf16x8* qr, int r32, int hi) {
;     p0 = f32x16{}; p1 = f32x16{};
; #pragma unroll
;     for (int d0 = 0; d0 < 8; ++d0) { const int cb = (d0 * 16 + hi * 8) * 2;
;         const bf16x8 b0 = *(LAS const bf16x8*)(Ks + ATT_KSWZ(r32, cb));
;         const bf16x8 b1 = *(LAS const bf16x8*)(Ks + ATT_KSWZ(32 + r32, cb));
;         p0 = __builtin_amdgcn_mfma_f32_32x32x16_bf16(b0, qr[d0], p0, 0, 0, 0);
;         p1 = __builtin_amdgcn_mfma_f32_32x32x16_bf16(b1, qr[d0], p1, 0, 0, 0); }
; }
; template <bool MOBA>
; __device__ __forceinline__ void run_unit(const UnitDesc& U, LAS unsigned char* lds, f32x16 (&o)[4], float (&rli)[16]) {
;     ...
;     const int sr = tid >> 4, sc = (tid & 15) * 8, vst0 = v_st(sr, sc), vst1 = v_st(32 + sr, sc), kst0 = ATT_KSWZ(sr, sc * 2), kst1 = ATT_KSWZ(32 + sr, sc * 2);
;     LAS const unsigned char* vb0 = V_lds + v_rd_base(lane);
;     const bf16_t* Kh = U.K + (size_t)(sr + kt0 * KVBLK) * NC + sc; const bf16_t* Vh = U.V + (size_t)(sr + kt0 * KVBLK) * NC + sc;
;     qpos -= kt0 * KVBLK; qlo -= kt0 * KVBLK;
;     bf16x8 sA_v0, sA_v1, sA_k0, sA_k1, sB_v0, sB_v1, sB_k0, sB_k1;
;     ...
;     f32x16 pA0, pA1, pB0, pB1; float mnA, mnB, alA, alB; bf16x8 pa0, pa1, pa2, pa3; const int NT = U.nt - kt0;
;     ATT_SLOAD(sA, 0); ATT_SLOAD(sB, KVBLK); ATT_SWAIT(); ATT_SWRITE(0, sA); __syncthreads();
;     qkt(pA0, pA1, K_lds, qr, r32, hi); ATT_PSM(pA0, pA1, mnA, alA, 0);
.LBB0_814:
	v_ashrrev_i32_e32 v5, 4, v8
	v_and_b32_e32 v7, 0xfffff0, v5
	v_lshlrev_b32_e32 v10, 1, v5
	v_lshlrev_b32_e32 v4, 3, v8
	v_and_or_b32 v7, v10, 8, v7
	v_lshrrev_b32_e32 v7, 1, v7
	v_bfe_u32 v11, v4, 5, 2
	v_and_b32_e32 v6, 0x78, v4
	v_or_b32_e32 v4, v7, v11
	v_lshrrev_b32_e32 v10, 1, v5
	v_lshlrev_b32_e32 v7, 9, v4
	v_and_b32_e32 v4, 3, v5
	v_and_or_b32 v4, v10, 4, v4
	v_lshlrev_b32_e32 v10, 6, v4
	v_lshlrev_b32_e32 v4, 1, v6
	v_and_b32_e32 v6, 48, v4
	v_or3_b32 v22, v7, v10, v6
	v_add_u32_e32 v7, 32, v5
	v_readlane_b32 s0, v254, 59
	v_and_b32_e32 v12, 0xfffff0, v7
	v_lshlrev_b32_e32 v13, 1, v7
	s_add_i32 s8, s66, s0
	s_lshl_b32 s0, s12, 1
	v_readlane_b32 s1, v254, 52
	v_and_or_b32 v12, v13, 8, v12
	s_add_u32 s0, s1, s0
	v_readlane_b32 s1, v254, 53
	v_lshrrev_b32_e32 v12, 1, v12
	s_addc_u32 s1, s1, 0
	s_lshl_b32 s6, s80, 7
	v_or_b32_e32 v11, v12, v11
	s_and_b32 s6, s6, 0x100
	v_readlane_b32 s7, v254, 54
	v_lshlrev_b32_e32 v11, 9, v11
	s_add_u32 s6, s7, s6
	v_readlane_b32 s7, v254, 55
	v_or3_b32 v23, v11, v10, v6
	v_lshlrev_b32_e32 v6, 8, v5
	v_and_b32_e32 v8, 0xf0, v8
	s_addc_u32 s7, s7, 0
	v_bitop3_b32 v24, v4, v6, v8 bitop3:0xde
	v_lshlrev_b32_e32 v6, 8, v7
	s_lshl_b32 s83, s82, 6
	v_bitop3_b32 v25, v4, v6, v8 bitop3:0xde
	v_add_u32_e32 v8, s83, v5
	v_mov_b64_e32 v[6:7], s[0:1]
	s_mov_b32 s9, 0xe800
	v_mad_i64_i32 v[6:7], s[0:1], v8, s9, v[6:7]
	v_mov_b32_e32 v5, v3
	v_lshl_add_u64 v[182:183], v[6:7], 0, v[4:5]
	v_mov_b64_e32 v[6:7], s[6:7]
	v_mad_i64_i32 v[6:7], s[0:1], v8, s9, v[6:7]
	v_lshl_add_u64 v[184:185], v[6:7], 0, v[4:5]
	s_mov_b32 s0, 0x1d0000
	v_add_co_u32_e32 v4, vcc, s0, v184
	v_or_b32_e32 v9, s8, v52
	s_nop 0
	v_addc_co_u32_e32 v5, vcc, 0, v185, vcc
	v_subrev_u32_e32 v190, s83, v9
	global_load_dwordx4 v[8:11], v[184:185], off
	global_load_dwordx4 v[12:15], v[4:5], off
	global_load_dwordx4 v[16:19], v[182:183], off
	v_add_co_u32_e32 v4, vcc, s0, v182
	s_mov_b32 s0, 0x3a0000
	s_nop 0
	v_addc_co_u32_e32 v5, vcc, 0, v183, vcc
	global_load_dwordx4 v[4:7], v[4:5], off
	v_add_co_u32_e32 v20, vcc, s0, v184
	s_mov_b32 s1, 0x570000
	s_nop 0
	v_addc_co_u32_e32 v21, vcc, 0, v185, vcc
	global_load_dwordx4 v[44:47], v[20:21], off
	v_add_co_u32_e32 v20, vcc, s1, v184
	v_add_u32_e32 v214, 0, v22
	s_nop 0
	v_addc_co_u32_e32 v21, vcc, 0, v185, vcc
	global_load_dwordx4 v[48:51], v[20:21], off
	v_add_co_u32_e32 v20, vcc, s0, v182
	v_add_u32_e32 v215, 0, v23
	s_nop 0
	v_addc_co_u32_e32 v21, vcc, 0, v183, vcc
	global_load_dwordx4 v[36:39], v[20:21], off
	v_add_co_u32_e32 v20, vcc, s1, v182
	v_add_u32_e32 v216, 0, v24
	s_nop 0
	v_addc_co_u32_e32 v21, vcc, 0, v183, vcc
	global_load_dwordx4 v[40:43], v[20:21], off
	v_add_u32_e32 v217, 0, v25
	s_waitcnt vmcnt(4)
	s_movk_i32 s0, 0xf0
	v_lshl_add_u32 v62, v52, 8, 0
	v_lshlrev_b32_e32 v202, 2, v1
	v_sub_u32_e32 v1, v190, v202
	v_mov_b32_e32 v197, v196
	s_sub_i32 s81, s8, s83
	s_cmp_gt_i32 s81, 62
	s_waitcnt vmcnt(7)
	ds_write_b128 v214, v[8:11]
	s_waitcnt vmcnt(6)
	ds_write_b128 v215, v[12:15]
	s_waitcnt vmcnt(5)
	ds_write_b128 v216, v[16:19] offset:32768
	s_waitcnt vmcnt(4)
	ds_write_b128 v217, v[4:7] offset:32768
	v_lshlrev_b32_e32 v4, 4, v52
	v_and_b32_e32 v53, 0xf0, v4
	v_bitop3_b32 v4, v2, v4, s0 bitop3:0x78
	v_add_u32_e32 v206, v62, v4
	s_waitcnt lgkmcnt(0)
	s_barrier
	ds_read_b128 v[4:7], v206 offset:32768
	ds_read_b128 v[8:11], v206 offset:40960
	s_waitcnt lgkmcnt(1)
	v_mfma_f32_32x32x16_bf16 v[20:35], v[4:7], v[142:145], 0
	v_bitop3_b32 v54, v2, v53, 32 bitop3:0x36
	v_add_u32_e32 v208, v62, v54
	ds_read_b128 v[54:57], v208 offset:32768
	ds_read_b128 v[58:61], v208 offset:40960
	s_movk_i32 s0, 0x60
	s_waitcnt lgkmcnt(2)
	v_mfma_f32_32x32x16_bf16 v[4:19], v[8:11], v[142:145], 0
	s_waitcnt lgkmcnt(1)
	v_mfma_f32_32x32x16_bf16 v[20:35], v[54:57], v[138:141], v[20:35]
	v_bitop3_b32 v54, v2, v53, 64 bitop3:0x36
	v_add_u32_e32 v204, v62, v54
	s_waitcnt lgkmcnt(0)
	v_mfma_f32_32x32x16_bf16 v[4:19], v[58:61], v[138:141], v[4:19]
	ds_read_b128 v[54:57], v204 offset:32768
	ds_read_b128 v[58:61], v204 offset:40960
	s_waitcnt lgkmcnt(1)
	v_mfma_f32_32x32x16_bf16 v[20:35], v[54:57], v[134:137], v[20:35]
	v_bitop3_b32 v54, v2, v53, s0 bitop3:0x36
	v_add_u32_e32 v209, v62, v54
	s_movk_i32 s0, 0x80
	s_waitcnt lgkmcnt(0)
	v_mfma_f32_32x32x16_bf16 v[4:19], v[58:61], v[134:137], v[4:19]
	ds_read_b128 v[54:57], v209 offset:32768
	ds_read_b128 v[58:61], v209 offset:40960
	s_waitcnt lgkmcnt(1)
	v_mfma_f32_32x32x16_bf16 v[20:35], v[54:57], v[130:133], v[20:35]
	v_bitop3_b32 v54, v2, v53, s0 bitop3:0x36
	v_add_u32_e32 v210, v62, v54
	s_movk_i32 s0, 0xa0
	s_waitcnt lgkmcnt(0)
	v_mfma_f32_32x32x16_bf16 v[4:19], v[58:61], v[130:133], v[4:19]
	ds_read_b128 v[54:57], v210 offset:32768
	ds_read_b128 v[58:61], v210 offset:40960
	s_waitcnt lgkmcnt(1)
	v_mfma_f32_32x32x16_bf16 v[20:35], v[54:57], v[126:129], v[20:35]
	v_bitop3_b32 v54, v2, v53, s0 bitop3:0x36
	v_add_u32_e32 v211, v62, v54
	s_movk_i32 s0, 0xc0
	s_waitcnt lgkmcnt(0)
	v_mfma_f32_32x32x16_bf16 v[4:19], v[58:61], v[126:129], v[4:19]
	ds_read_b128 v[54:57], v211 offset:32768
	ds_read_b128 v[58:61], v211 offset:40960
	s_waitcnt lgkmcnt(1)
	v_mfma_f32_32x32x16_bf16 v[20:35], v[54:57], v[122:125], v[20:35]
	v_bitop3_b32 v54, v2, v53, s0 bitop3:0x36
	v_add_u32_e32 v212, v62, v54
	s_movk_i32 s0, 0xe0
	v_bitop3_b32 v2, v2, v53, s0 bitop3:0x36
	v_add_u32_e32 v213, v62, v2
	v_cvt_f32_i32_e32 v53, v1
	s_mov_b32 s0, 2.0
	s_waitcnt lgkmcnt(0)
	v_mfma_f32_32x32x16_bf16 v[4:19], v[58:61], v[122:125], v[4:19]
	ds_read_b128 v[54:57], v212 offset:32768
	ds_read_b128 v[58:61], v212 offset:40960
	v_mul_f32_e64 v2, -v196, v53
	s_mov_b32 s1, 0x40400000
	v_fma_f32 v66, v198, s86, v2
	v_fma_f32 v67, v199, s87, v2
	v_pk_fma_f32 v[68:69], v[198:199], s[88:89], v[2:3] op_sel_hi:[1,1,0]
	s_waitcnt lgkmcnt(1)
; #define LAS __attribute__((address_space(3)))
; __device__ __forceinline__ void qkt(f32x16& p0, f32x16& p1, LAS const unsigned char* Ks, const bf16x8* qr, int r32, int hi) {
;     p0 = f32x16{}; p1 = f32x16{};
; #pragma unroll
;     for (int d0 = 0; d0 < 8; ++d0) { const int cb = (d0 * 16 + hi * 8) * 2;
;         const bf16x8 b0 = *(LAS const bf16x8*)(Ks + ATT_KSWZ(r32, cb));
;         const bf16x8 b1 = *(LAS const bf16x8*)(Ks + ATT_KSWZ(32 + r32, cb));
;         p0 = __builtin_amdgcn_mfma_f32_32x32x16_bf16(b0, qr[d0], p0, 0, 0, 0);
;         p1 = __builtin_amdgcn_mfma_f32_32x32x16_bf16(b1, qr[d0], p1, 0, 0, 0); }
; }
; __device__ __forceinline__ void partialSM(f32x16& p0, f32x16& p1, float& m_reg, float& mn, float& alpha, int dq, float slopeL, bool diag, bool rowmasked) {
;     const float NEG = -__builtin_inff(); const float a0 = -slopeL * (float)dq;
; #pragma unroll
;     for (int r = 0; r < 16; ++r) { const int c = (r & 3) + 8 * (r >> 2);
;         p0[r] = fmaf(p0[r], CS, fmaf(slopeL, (float)c, a0)); p1[r] = fmaf(p1[r], CS, fmaf(slopeL, (float)(c + 32), a0)); }
;     if (diag) { asm volatile("" ::: "memory");
; #pragma unroll
;         for (int r = 0; r < 16; ++r) { const int c = (r & 3) + 8 * (r >> 2); if (c > dq) p0[r] = NEG; if (c + 32 > dq) p1[r] = NEG; } }
	v_mfma_f32_32x32x16_bf16 v[20:35], v[54:57], v[118:121], v[20:35]
	s_waitcnt lgkmcnt(0)
	v_mfma_f32_32x32x16_bf16 v[4:19], v[58:61], v[118:121], v[4:19]
	ds_read_b128 v[54:57], v213 offset:32768
	ds_read_b128 v[58:61], v213 offset:40960
	s_waitcnt lgkmcnt(1)
	v_mfma_f32_32x32x16_bf16 v[20:35], v[54:57], v[114:117], v[20:35]
	v_fma_f32 v56, v198, s0, v2
	v_fma_f32 v57, v199, s1, v2
	s_mov_b32 s0, 0x41000000
	s_mov_b32 s1, 0x41100000
	v_mov_b32_e32 v54, v2
	v_fma_f32 v55, -v196, v53, v196
	v_fmac_f32_e32 v54, 0, v196
	s_nop 4
	v_pk_fma_f32 v[34:35], v[34:35], s[96:97], v[68:69] op_sel_hi:[1,0,1]
	s_waitcnt lgkmcnt(0)
	v_mfma_f32_32x32x16_bf16 v[4:19], v[58:61], v[114:117], v[4:19]
	v_fma_f32 v58, v198, s0, v2
	v_fma_f32 v59, v199, s1, v2
	s_mov_b32 s0, 0x41200000
	s_mov_b32 s1, 0x41300000
	v_fma_f32 v60, v198, s0, v2
	v_fma_f32 v61, v199, s1, v2
	s_mov_b32 s0, 0x41800000
	s_mov_b32 s1, 0x41880000
	v_pk_fma_f32 v[62:63], v[198:199], s[0:1], v[2:3] op_sel_hi:[1,1,0]
	s_mov_b32 s0, 0x41900000
	s_mov_b32 s1, 0x41980000
	v_pk_fma_f32 v[64:65], v[198:199], s[0:1], v[2:3] op_sel_hi:[1,1,0]
	v_pk_fma_f32 v[32:33], v[32:33], s[96:97], v[66:67] op_sel_hi:[1,0,1]
	v_pk_fma_f32 v[30:31], v[30:31], s[96:97], v[64:65] op_sel_hi:[1,0,1]
	v_pk_fma_f32 v[28:29], v[28:29], s[96:97], v[62:63] op_sel_hi:[1,0,1]
	v_pk_fma_f32 v[26:27], v[26:27], s[96:97], v[60:61] op_sel_hi:[1,0,1]
	v_pk_fma_f32 v[24:25], v[24:25], s[96:97], v[58:59] op_sel_hi:[1,0,1]
	v_pk_fma_f32 v[22:23], v[22:23], s[96:97], v[56:57] op_sel_hi:[1,0,1]
	v_pk_fma_f32 v[20:21], v[20:21], s[96:97], v[54:55] op_sel_hi:[1,0,1]
	v_pk_fma_f32 v[54:55], v[200:201], s[76:77], v[2:3] op_sel_hi:[1,1,0]
	v_pk_fma_f32 v[56:57], v[196:197], s[90:91], v[2:3] op_sel_hi:[1,1,0]
	v_pk_fma_f32 v[58:59], v[196:197], s[92:93], v[2:3] op_sel_hi:[1,1,0]
	v_pk_fma_f32 v[60:61], v[196:197], s[94:95], v[2:3] op_sel_hi:[1,1,0]
	v_pk_fma_f32 v[62:63], v[196:197], s[68:69], v[2:3] op_sel_hi:[1,1,0]
	v_pk_fma_f32 v[64:65], v[196:197], s[70:71], v[2:3] op_sel_hi:[1,1,0]
	v_pk_fma_f32 v[66:67], v[196:197], s[72:73], v[2:3] op_sel_hi:[1,1,0]
	v_pk_fma_f32 v[68:69], v[196:197], s[74:75], v[2:3] op_sel_hi:[1,1,0]
	v_pk_fma_f32 v[16:17], v[16:17], s[96:97], v[66:67] op_sel_hi:[1,0,1]
	v_pk_fma_f32 v[18:19], v[18:19], s[96:97], v[68:69] op_sel_hi:[1,0,1]
	v_pk_fma_f32 v[14:15], v[14:15], s[96:97], v[64:65] op_sel_hi:[1,0,1]
	v_pk_fma_f32 v[12:13], v[12:13], s[96:97], v[62:63] op_sel_hi:[1,0,1]
	v_pk_fma_f32 v[10:11], v[10:11], s[96:97], v[60:61] op_sel_hi:[1,0,1]
	v_pk_fma_f32 v[8:9], v[8:9], s[96:97], v[58:59] op_sel_hi:[1,0,1]
	v_pk_fma_f32 v[6:7], v[6:7], s[96:97], v[56:57] op_sel_hi:[1,0,1]
	v_pk_fma_f32 v[4:5], v[4:5], s[96:97], v[54:55] op_sel_hi:[1,0,1]
	s_cbranch_scc1 .LBB0_818
	v_cmp_gt_i32_e64 s[62:63], 57, v1
	v_cmp_gt_i32_e64 s[64:65], 58, v1
	v_cmp_gt_i32_e64 s[60:61], 56, v1
	s_and_b64 s[62:63], s[64:65], s[62:63]
	v_cmp_gt_i32_e64 s[58:59], 51, v1
	s_and_b64 s[60:61], s[62:63], s[60:61]
	v_cmp_gt_i32_e64 s[56:57], 50, v1
	s_and_b64 s[58:59], s[60:61], s[58:59]
	v_cmp_gt_i32_e64 s[54:55], 49, v1
	s_and_b64 s[56:57], s[58:59], s[56:57]
	v_cmp_gt_i32_e64 s[52:53], 48, v1
	s_and_b64 s[54:55], s[56:57], s[54:55]
	v_cmp_gt_i32_e64 s[50:51], 43, v1
	s_and_b64 s[52:53], s[54:55], s[52:53]
	v_cmp_gt_i32_e64 s[48:49], 42, v1
	s_and_b64 s[50:51], s[52:53], s[50:51]
	v_cmp_gt_i32_e64 s[46:47], 41, v1
	s_and_b64 s[48:49], s[50:51], s[48:49]
	v_cmp_gt_i32_e64 s[44:45], 40, v1
	s_and_b64 s[46:47], s[48:49], s[46:47]
	v_cmp_gt_i32_e64 s[42:43], 35, v1
	s_and_b64 s[44:45], s[46:47], s[44:45]
	v_cmp_gt_i32_e64 s[40:41], 34, v1
	s_and_b64 s[42:43], s[44:45], s[42:43]
	v_cmp_gt_i32_e64 s[38:39], 33, v1
	s_and_b64 s[40:41], s[42:43], s[40:41]
	v_cmp_gt_i32_e64 s[36:37], 32, v1
	s_and_b64 s[38:39], s[40:41], s[38:39]
	s_and_b64 s[36:37], s[38:39], s[36:37]
	v_cmp_gt_i32_e32 vcc, 0, v1
	v_cmp_gt_i32_e64 s[0:1], 1, v1
	v_cmp_gt_i32_e64 s[6:7], 2, v1
	v_cmp_gt_i32_e64 s[8:9], 3, v1
	v_cmp_gt_i32_e64 s[10:11], 8, v1
	v_cmp_gt_i32_e64 s[14:15], 9, v1
	v_cmp_gt_i32_e64 s[16:17], 10, v1
	v_cmp_gt_i32_e64 s[18:19], 11, v1
	v_cmp_gt_i32_e64 s[20:21], 16, v1
	v_cmp_gt_i32_e64 s[22:23], 17, v1
	v_cmp_gt_i32_e64 s[24:25], 18, v1
	v_cmp_gt_i32_e64 s[26:27], 19, v1
	v_cmp_gt_i32_e64 s[28:29], 24, v1
	v_cmp_gt_i32_e64 s[30:31], 25, v1
	v_cmp_gt_i32_e64 s[34:35], 26, v1
	v_cndmask_b32_e64 v18, v18, v241, s[64:65]
	v_cndmask_b32_e64 v17, v17, v241, s[62:63]
	v_cndmask_b32_e64 v16, v16, v241, s[60:61]
	v_cndmask_b32_e64 v15, v15, v241, s[58:59]
	v_cndmask_b32_e64 v14, v14, v241, s[56:57]
	v_cndmask_b32_e64 v13, v13, v241, s[54:55]
	v_cndmask_b32_e64 v12, v12, v241, s[52:53]
	v_cndmask_b32_e64 v11, v11, v241, s[50:51]
	v_cndmask_b32_e64 v10, v10, v241, s[48:49]
	v_cndmask_b32_e64 v9, v9, v241, s[46:47]
	v_cndmask_b32_e64 v8, v8, v241, s[44:45]
	v_cndmask_b32_e64 v7, v7, v241, s[42:43]
	v_cndmask_b32_e64 v6, v6, v241, s[40:41]
	v_cndmask_b32_e64 v5, v5, v241, s[38:39]
	v_cndmask_b32_e64 v4, v4, v241, s[36:37]
	v_cmp_gt_i32_e64 s[36:37], 27, v1
	v_cmp_gt_i32_e64 s[38:39], 59, v1
	s_and_saveexec_b64 s[12:13], s[38:39]
	v_mov_b32_e32 v19, s85
	s_or_b64 exec, exec, s[12:13]
	s_and_b64 s[34:35], s[36:37], s[34:35]
	s_and_b64 s[30:31], s[34:35], s[30:31]
	s_and_b64 s[28:29], s[30:31], s[28:29]
	s_and_b64 s[26:27], s[28:29], s[26:27]
	s_and_b64 s[24:25], s[26:27], s[24:25]
	s_and_b64 s[22:23], s[24:25], s[22:23]
	s_and_b64 s[20:21], s[22:23], s[20:21]
	s_and_b64 s[18:19], s[20:21], s[18:19]
	s_and_b64 s[16:17], s[18:19], s[16:17]
	s_and_b64 s[14:15], s[16:17], s[14:15]
	s_and_b64 s[10:11], s[14:15], s[10:11]
	s_and_b64 s[8:9], s[10:11], s[8:9]
	s_and_b64 s[6:7], s[8:9], s[6:7]
	s_and_b64 s[0:1], s[6:7], s[0:1]
	s_and_b64 vcc, s[0:1], vcc
	v_cndmask_b32_e64 v34, v34, v241, s[34:35]
	v_cndmask_b32_e64 v33, v33, v241, s[30:31]
	v_cndmask_b32_e64 v32, v32, v241, s[28:29]
	v_cndmask_b32_e64 v31, v31, v241, s[26:27]
	v_cndmask_b32_e64 v30, v30, v241, s[24:25]
	v_cndmask_b32_e64 v29, v29, v241, s[22:23]
	v_cndmask_b32_e64 v28, v28, v241, s[20:21]
	v_cndmask_b32_e64 v27, v27, v241, s[18:19]
	v_cndmask_b32_e64 v26, v26, v241, s[16:17]
	v_cndmask_b32_e64 v25, v25, v241, s[14:15]
	v_cndmask_b32_e64 v24, v24, v241, s[10:11]
	v_cndmask_b32_e64 v23, v23, v241, s[8:9]
	v_cndmask_b32_e64 v22, v22, v241, s[6:7]
	v_cndmask_b32_e64 v21, v21, v241, s[0:1]
	v_cndmask_b32_e32 v20, v20, v241, vcc
	v_cndmask_b32_e64 v35, v35, v241, s[36:37]
